# v29 + rewritten grid barrier; XCD-local group barriers at the seams out-proj->logits, logits->cross-attn-out, mlp1->mlp2 (dependencies stay inside one batch/XCD group)
# speedup vs baseline: 1.0130x; 1.0094x over previous
_Z3fwd4Args:
	s_mov_b32 s100, 0
	v_writelane_b32 v255, s100, 62
	s_mov_b64 s[58:59], s[0:1]
	s_load_dwordx8 s[80:87], s[0:1], 0x110
	s_load_dword s3, s[0:1], 0x130
	s_add_u32 s4, s58, 0x130
	s_addc_u32 s5, s59, 0
	v_lshl_add_u32 v1, v0, 2, 0
	v_writelane_b32 v251, s4, 0
	v_readfirstlane_b32 s0, v0
	v_add_u32_e32 v1, 0x20800, v1
	v_writelane_b32 v251, s5, 1
	s_mov_b32 s4, 0
	s_mov_b32 s5, 1
	s_mov_b64 s[6:7], 0
	v_mov_b32_e32 v2, 0
	s_mov_b32 s8, s4
	s_branch .LBB0_2

.LBB0_217:
	v_readlane_b32 s0, v253, 45
	v_readlane_b32 s1, v253, 46
	v_mov_b32_e32 v3, 1
	s_waitcnt lgkmcnt(0)
	s_nop 4
	global_atomic_add v3, v129, v3, s[0:1] sc0
	v_cvt_f32_u32_e32 v4, v2
	v_sub_u32_e32 v1, 0, v2
	v_rcp_iflag_f32_e32 v4, v4
	s_nop 1
	v_mul_f32_e32 v4, 0x4f7ffffe, v4
	v_cvt_u32_f32_e32 v4, v4
	v_mul_lo_u32 v1, v1, v4
	v_mul_hi_u32 v1, v4, v1
	v_add_u32_e32 v1, v4, v1
	v_readlane_b32 s8, v255, 62
	s_nop 3
	s_add_i32 s8, s8, 1
	s_nop 1
	v_writelane_b32 v255, s8, 62
	v_mul_lo_u32 v4, s8, v0
	s_waitcnt vmcnt(0)
	v_mul_hi_u32 v1, v3, v1
	v_mul_lo_u32 v5, v1, v2
	v_sub_u32_e32 v5, v3, v5
	v_cmp_ge_u32_e32 vcc, v5, v2
	s_nop 1
	v_addc_co_u32_e32 v1, vcc, 0, v1, vcc
	v_mul_lo_u32 v5, v1, v2
	v_sub_u32_e32 v5, v3, v5
	v_cmp_ge_u32_e32 vcc, v5, v2
	s_nop 1
	v_addc_co_u32_e32 v1, vcc, 0, v1, vcc
	v_add_u32_e32 v5, 1, v1
	v_mul_lo_u32 v5, v5, v2
	v_add_u32_e32 v3, 1, v3
	v_readlane_b32 s0, v253, 49
	v_readlane_b32 s1, v253, 50
	v_cmp_ne_u32_e32 vcc, v3, v5
	s_nop 3
	s_cbranch_vccnz .Lxb0_poll
	buffer_wbl2 sc1
	s_waitcnt vmcnt(0)
	v_mov_b32_e32 v3, 1
	global_atomic_add v129, v3, s[0:1]

.LBB0_371:
	v_readlane_b32 s8, v253, 45
	v_readlane_b32 s9, v253, 46
	v_mov_b32_e32 v3, 1
	s_waitcnt lgkmcnt(0)
	s_nop 4
	global_atomic_add v3, v129, v3, s[8:9] sc0
	v_cvt_f32_u32_e32 v4, v2
	v_sub_u32_e32 v1, 0, v2
	v_rcp_iflag_f32_e32 v4, v4
	s_nop 1
	v_mul_f32_e32 v4, 0x4f7ffffe, v4
	v_cvt_u32_f32_e32 v4, v4
	v_mul_lo_u32 v1, v1, v4
	v_mul_hi_u32 v1, v4, v1
	v_add_u32_e32 v1, v4, v1
	v_readlane_b32 s1, v255, 62
	s_nop 3
	s_add_i32 s1, s1, 1
	s_nop 1
	v_writelane_b32 v255, s1, 62
	v_mul_lo_u32 v4, s1, v0
	s_waitcnt vmcnt(0)
	v_mul_hi_u32 v1, v3, v1
	v_mul_lo_u32 v5, v1, v2
	v_sub_u32_e32 v5, v3, v5
	v_cmp_ge_u32_e32 vcc, v5, v2
	s_nop 1
	v_addc_co_u32_e32 v1, vcc, 0, v1, vcc
	v_mul_lo_u32 v5, v1, v2
	v_sub_u32_e32 v5, v3, v5
	v_cmp_ge_u32_e32 vcc, v5, v2
	s_nop 1
	v_addc_co_u32_e32 v1, vcc, 0, v1, vcc
	v_add_u32_e32 v5, 1, v1
	v_mul_lo_u32 v5, v5, v2
	v_add_u32_e32 v3, 1, v3
	v_readlane_b32 s8, v253, 49
	v_readlane_b32 s9, v253, 50
	v_cmp_ne_u32_e32 vcc, v3, v5
	s_nop 3
	s_cbranch_vccnz .Lxb1_poll
	buffer_wbl2 sc1
	s_waitcnt vmcnt(0)
	v_mov_b32_e32 v3, 1
	global_atomic_add v129, v3, s[8:9]

.LBB0_1373:
	v_readlane_b32 s8, v253, 45
	v_readlane_b32 s9, v253, 46
	v_mov_b32_e32 v3, 1
	s_waitcnt lgkmcnt(0)
	s_nop 4
	global_atomic_add v3, v129, v3, s[8:9] sc0
	v_cvt_f32_u32_e32 v4, v2
	v_sub_u32_e32 v1, 0, v2
	v_rcp_iflag_f32_e32 v4, v4
	s_nop 1
	v_mul_f32_e32 v4, 0x4f7ffffe, v4
	v_cvt_u32_f32_e32 v4, v4
	v_mul_lo_u32 v1, v1, v4
	v_mul_hi_u32 v1, v4, v1
	v_add_u32_e32 v1, v4, v1
	s_waitcnt vmcnt(0)
	v_mul_hi_u32 v1, v3, v1
	v_mul_lo_u32 v5, v1, v2
	v_sub_u32_e32 v5, v3, v5
	v_cmp_ge_u32_e32 vcc, v5, v2
	s_nop 1
	v_addc_co_u32_e32 v1, vcc, 0, v1, vcc
	v_mul_lo_u32 v5, v1, v2
	v_sub_u32_e32 v5, v3, v5
	v_cmp_ge_u32_e32 vcc, v5, v2
	s_nop 1
	v_addc_co_u32_e32 v1, vcc, 0, v1, vcc
	v_add_u32_e32 v5, 1, v1
	v_mul_lo_u32 v5, v5, v2
	v_add_u32_e32 v3, 1, v3
	s_mov_b32 s1, 0
.Lxb7_spin:
	global_load_dword v3, v129, s[8:9] sc1
	s_waitcnt vmcnt(0)
	v_cmp_ge_u32_e32 vcc, v3, v5
	s_cbranch_vccnz .Lxb7_done
	s_sleep 1
	s_add_i32 s1, s1, 1
	s_cmp_lt_u32 s1, 0x40000
	s_cbranch_scc1 .Lxb7_spin
